# attention QK^T: K/Q fragment LDS reads renamed onto the section's own register quads and issued a window ahead (was one LDS round trip per MFMA), counted lgkmcnt waits
# speedup vs baseline: 1.0095x; 1.0095x over previous
.LBB0_3234:
	s_waitcnt vmcnt(0)
	ds_read_b128 v[4:7], v198 offset:49152
	ds_read_b128 v[8:11], v198 offset:57344
	ds_read_b128 v[12:15], v204 offset:49152
	ds_read_b128 v[20:23], v204 offset:57344
	ds_read_b128 v[24:27], v205 offset:49152
	ds_read_b128 v[28:31], v205 offset:57344
	ds_read_b128 v[178:181], v206 offset:49152
	ds_read_b128 v[216:219], v206 offset:57344
	ds_read_b128 v[228:231], v198 offset:49280
	ds_read_b128 v[232:235], v191 offset:4096
	s_waitcnt lgkmcnt(9)
	v_mfma_f32_32x32x16_bf16 v[114:129], v[4:7], v[174:177], 0
	ds_read_b128 v[4:7], v198 offset:57472
	s_waitcnt lgkmcnt(9)
	v_mfma_f32_32x32x16_bf16 v[98:113], v[8:11], v[174:177], 0
	ds_read_b128 v[8:11], v204 offset:49280
	s_waitcnt lgkmcnt(9)
	v_mfma_f32_32x32x16_bf16 v[114:129], v[12:15], v[170:173], v[114:129]
	ds_read_b128 v[12:15], v191 offset:5120
	s_waitcnt lgkmcnt(9)
	v_mfma_f32_32x32x16_bf16 v[98:113], v[20:23], v[170:173], v[98:113]
	ds_read_b128 v[20:23], v204 offset:57472
	s_waitcnt lgkmcnt(9)
	v_mfma_f32_32x32x16_bf16 v[114:129], v[24:27], v[166:169], v[114:129]
	ds_read_b128 v[24:27], v205 offset:49280
	s_waitcnt lgkmcnt(9)
	v_mfma_f32_32x32x16_bf16 v[98:113], v[28:31], v[166:169], v[98:113]
	ds_read_b128 v[28:31], v191 offset:6144
	s_waitcnt lgkmcnt(9)
	v_mfma_f32_32x32x16_bf16 v[114:129], v[178:181], v[162:165], v[114:129]
	ds_read_b128 v[178:181], v205 offset:57472
	s_waitcnt lgkmcnt(9)
	v_mfma_f32_32x32x16_bf16 v[98:113], v[216:219], v[162:165], v[98:113]
	ds_read_b128 v[216:219], v206 offset:49280
	s_waitcnt lgkmcnt(8)
	v_mfma_f32_32x32x16_bf16 v[114:129], v[228:231], v[232:235], v[114:129]
	ds_read_b128 v[228:231], v191 offset:7168
	s_waitcnt lgkmcnt(8)
	v_mfma_f32_32x32x16_bf16 v[98:113], v[4:7], v[232:235], v[98:113]
	ds_read_b128 v[4:7], v206 offset:57472
	s_waitcnt lgkmcnt(7)
	v_mfma_f32_32x32x16_bf16 v[114:129], v[8:11], v[12:15], v[114:129]
	s_waitcnt lgkmcnt(6)
	v_mfma_f32_32x32x16_bf16 v[98:113], v[20:23], v[12:15], v[98:113]
	s_waitcnt lgkmcnt(4)
	v_mfma_f32_32x32x16_bf16 v[114:129], v[24:27], v[28:31], v[114:129]
	s_waitcnt lgkmcnt(3)
	v_mfma_f32_32x32x16_bf16 v[98:113], v[178:181], v[28:31], v[98:113]
	s_waitcnt lgkmcnt(1)
	v_mfma_f32_32x32x16_bf16 v[114:129], v[216:219], v[228:231], v[114:129]
	s_waitcnt lgkmcnt(0)
	v_mfma_f32_32x32x16_bf16 v[98:113], v[4:7], v[228:231], v[98:113]
	s_branch .LBB0_3238

.LBB0_3264:
	ds_read_b128 v[20:23], v198 offset:32768
	ds_read_b128 v[24:27], v198 offset:40960
	ds_read_b128 v[28:31], v204 offset:32768
	ds_read_b128 v[218:221], v204 offset:40960
	ds_read_b128 v[228:231], v205 offset:32768
	ds_read_b128 v[232:235], v205 offset:40960
	ds_read_b128 v[236:239], v206 offset:32768
	ds_read_b128 v[240:243], v206 offset:40960
	ds_read_b128 v[244:247], v198 offset:32896
	ds_read_b128 v[250:253], v191 offset:4096
	s_waitcnt lgkmcnt(9)
	v_mfma_f32_32x32x16_bf16 v[114:129], v[20:23], v[174:177], 0
	ds_read_b128 v[20:23], v198 offset:41088
	s_waitcnt lgkmcnt(9)
	v_mfma_f32_32x32x16_bf16 v[98:113], v[24:27], v[174:177], 0
	ds_read_b128 v[24:27], v204 offset:32896
	s_waitcnt lgkmcnt(9)
	v_mfma_f32_32x32x16_bf16 v[114:129], v[28:31], v[170:173], v[114:129]
	ds_read_b128 v[28:31], v191 offset:5120
	s_waitcnt lgkmcnt(9)
	v_mfma_f32_32x32x16_bf16 v[98:113], v[218:221], v[170:173], v[98:113]
	ds_read_b128 v[218:221], v204 offset:41088
	s_waitcnt lgkmcnt(9)
	v_mfma_f32_32x32x16_bf16 v[114:129], v[228:231], v[166:169], v[114:129]
	ds_read_b128 v[228:231], v205 offset:32896
	s_waitcnt lgkmcnt(9)
	v_mfma_f32_32x32x16_bf16 v[98:113], v[232:235], v[166:169], v[98:113]
	ds_read_b128 v[232:235], v191 offset:6144
	s_waitcnt lgkmcnt(9)
	v_mfma_f32_32x32x16_bf16 v[114:129], v[236:239], v[162:165], v[114:129]
	ds_read_b128 v[236:239], v205 offset:41088
	s_waitcnt lgkmcnt(9)
	v_mfma_f32_32x32x16_bf16 v[98:113], v[240:243], v[162:165], v[98:113]
	ds_read_b128 v[240:243], v206 offset:32896
	s_waitcnt lgkmcnt(8)
	v_mfma_f32_32x32x16_bf16 v[114:129], v[244:247], v[250:253], v[114:129]
	ds_read_b128 v[244:247], v191 offset:7168
	s_waitcnt lgkmcnt(8)
	v_mfma_f32_32x32x16_bf16 v[98:113], v[20:23], v[250:253], v[98:113]
	ds_read_b128 v[20:23], v206 offset:41088
	s_waitcnt lgkmcnt(7)
	v_mfma_f32_32x32x16_bf16 v[114:129], v[24:27], v[28:31], v[114:129]
	s_waitcnt lgkmcnt(6)
	v_mfma_f32_32x32x16_bf16 v[98:113], v[218:221], v[28:31], v[98:113]
	s_waitcnt lgkmcnt(4)
	v_mfma_f32_32x32x16_bf16 v[114:129], v[228:231], v[232:235], v[114:129]
	s_waitcnt lgkmcnt(3)
	v_mfma_f32_32x32x16_bf16 v[98:113], v[236:239], v[232:235], v[98:113]
	s_waitcnt lgkmcnt(1)
	v_mfma_f32_32x32x16_bf16 v[114:129], v[240:243], v[244:247], v[114:129]
	s_waitcnt lgkmcnt(0)
	v_mfma_f32_32x32x16_bf16 v[98:113], v[20:23], v[244:247], v[98:113]
	s_branch .LBB0_3268

.LBB0_3295:
	ds_read_b128 v[4:7], v198 offset:49152
	ds_read_b128 v[8:11], v198 offset:57344
	ds_read_b128 v[12:15], v204 offset:49152
	ds_read_b128 v[20:23], v204 offset:57344
	ds_read_b128 v[24:27], v205 offset:49152
	ds_read_b128 v[28:31], v205 offset:57344
	s_waitcnt lgkmcnt(5)
	v_mfma_f32_32x32x16_bf16 v[114:129], v[4:7], v[174:177], 0
	ds_read_b128 v[4:7], v206 offset:49152
	s_waitcnt lgkmcnt(5)
	v_mfma_f32_32x32x16_bf16 v[98:113], v[8:11], v[174:177], 0
	ds_read_b128 v[8:11], v206 offset:57344
	ds_read_b128 v[174:177], v198 offset:49280
	s_waitcnt lgkmcnt(6)
	v_mfma_f32_32x32x16_bf16 v[114:129], v[12:15], v[170:173], v[114:129]
	ds_read_b128 v[12:15], v191 offset:4096
	s_waitcnt lgkmcnt(6)
	v_mfma_f32_32x32x16_bf16 v[98:113], v[20:23], v[170:173], v[98:113]
	ds_read_b128 v[20:23], v198 offset:57472
	ds_read_b128 v[170:173], v204 offset:49280
	s_waitcnt lgkmcnt(7)
	v_mfma_f32_32x32x16_bf16 v[114:129], v[24:27], v[166:169], v[114:129]
	ds_read_b128 v[24:27], v191 offset:5120
	s_waitcnt lgkmcnt(7)
	v_mfma_f32_32x32x16_bf16 v[98:113], v[28:31], v[166:169], v[98:113]
	ds_read_b128 v[28:31], v204 offset:57472
	ds_read_b128 v[166:169], v205 offset:49280
	s_waitcnt lgkmcnt(8)
	v_mfma_f32_32x32x16_bf16 v[114:129], v[4:7], v[162:165], v[114:129]
	ds_read_b128 v[4:7], v191 offset:6144
	s_waitcnt lgkmcnt(8)
	v_mfma_f32_32x32x16_bf16 v[98:113], v[8:11], v[162:165], v[98:113]
	ds_read_b128 v[8:11], v205 offset:57472
	ds_read_b128 v[162:165], v206 offset:49280
	s_waitcnt lgkmcnt(8)
	v_mfma_f32_32x32x16_bf16 v[114:129], v[174:177], v[12:15], v[114:129]
	ds_read_b128 v[174:177], v191 offset:7168
	s_waitcnt lgkmcnt(8)
	v_mfma_f32_32x32x16_bf16 v[98:113], v[20:23], v[12:15], v[98:113]
	ds_read_b128 v[20:23], v206 offset:57472
	s_waitcnt lgkmcnt(7)
	v_mfma_f32_32x32x16_bf16 v[114:129], v[170:173], v[24:27], v[114:129]
	s_waitcnt lgkmcnt(6)
	v_mfma_f32_32x32x16_bf16 v[98:113], v[28:31], v[24:27], v[98:113]
	s_waitcnt lgkmcnt(4)
	v_mfma_f32_32x32x16_bf16 v[114:129], v[166:169], v[4:7], v[114:129]
	s_waitcnt lgkmcnt(3)
	v_mfma_f32_32x32x16_bf16 v[98:113], v[8:11], v[4:7], v[98:113]
	s_waitcnt lgkmcnt(1)
	v_mfma_f32_32x32x16_bf16 v[114:129], v[162:165], v[174:177], v[114:129]
	s_waitcnt lgkmcnt(0)
	v_mfma_f32_32x32x16_bf16 v[98:113], v[20:23], v[174:177], v[98:113]
	s_branch .LBB0_3299
